# hyena filter final stage (h2 @ hy_w3) on f32 matrix cores v_mfma_f32_32x32x2_f32 instead of LDS-broadcast f32 FMAs; h2 LDS pitch 65
# speedup vs baseline: 1.0099x; 1.0006x over previous
.LBB0_108:
	s_or_b64 exec, exec, s[0:1]
	v_mul_f32_e32 v39, v38, v38
	v_fmamk_f32 v40, v39, 0xb94c1982, v45
	v_fmaak_f32 v40, v39, v40, 0xbe2aaa9d
	v_mul_f32_e32 v40, v39, v40
	v_fmac_f32_e32 v38, v38, v40
	v_fmamk_f32 v40, v39, 0x37d75334, v46
	v_fmaak_f32 v40, v39, v40, 0x3d2aabf7
	v_fmaak_f32 v40, v39, v40, 0xbf000004
	v_fma_f32 v39, v39, v40, 1.0
	v_and_b32_e32 v40, 1, v37
	v_lshlrev_b32_e32 v37, 30, v37
	v_cmp_eq_u32_e32 vcc, 0, v40
	v_and_b32_e32 v37, 0x80000000, v37
	v_xor_b32_e32 v36, v36, v35
	v_cndmask_b32_e32 v38, v39, v38, vcc
	v_xor_b32_e32 v36, v36, v37
	v_xor_b32_e32 v36, v36, v38
	v_cmp_class_f32_e64 vcc, v35, s73
	s_nop 1
	v_cndmask_b32_e32 v35, v52, v36, vcc
	v_lshrrev_b32_e32 v36, 6, v13
	v_add_u32_e32 v36, v36, v13
	v_lshlrev_b32_e32 v36, 2, v36
	ds_write_b32 v36, v35 offset:12800
	v_add_u32_e32 v35, 0x200, v13
	v_cmp_lt_i32_e32 vcc, s88, v13
	s_or_b64 s[66:67], vcc, s[66:67]
	v_mov_b32_e32 v13, v35
	s_andn2_b64 exec, exec, s[66:67]
	s_cbranch_execz .LBB0_115

.LBB0_116:
	s_or_b64 exec, exec, s[62:63]
	s_add_i32 s0, s96, -1
	v_mov_b64_e32 v[34:35], s[2:3]
	s_and_b64 s[10:11], s[58:59], exec
	v_mad_u64_u32 v[34:35], s[10:11], v36, s91, v[34:35]
	v_mul_lo_u32 v13, v37, s91
	s_cselect_b32 s1, 9, 12
	v_add_u32_e32 v35, v13, v35
	s_cselect_b32 s28, 0x400000, 0
	v_lshlrev_b64 v[38:39], s1, v[2:3]
	v_lshl_add_u64 v[34:35], v[34:35], 0, s[28:29]
	v_lshlrev_b64 v[38:39], 1, v[38:39]
	v_lshl_add_u64 v[34:35], v[34:35], 0, v[38:39]
	s_mov_b32 s1, s29
	v_mov_b64_e32 v[40:41], s[28:29]
	v_lshlrev_b64 v[32:33], 18, v[36:37]
	v_cvt_f32_u32_e32 v9, s0
	v_lshl_add_u64 v[34:35], s[0:1], 1, v[34:35]
	v_mad_u64_u32 v[36:37], s[0:1], v36, s91, v[40:41]
	v_add_u32_e32 v37, v13, v37
	v_lshl_add_u64 v[38:39], v[36:37], 0, v[38:39]
	s_lshl_b32 s28, s96, 1
	s_ashr_i32 s57, s56, 31
	v_lshl_add_u64 v[36:37], v[38:39], 0, s[28:29]
	s_lshl_b64 s[0:1], s[56:57], 1
	v_subrev_co_u32_e32 v36, vcc, s0, v36
	s_add_u32 s0, s56, s96
	v_mov_b32_e32 v13, s1
	s_addc_u32 s1, s57, 0
	s_lshl_b64 s[0:1], s[0:1], 1
	s_add_u32 s0, s20, s0
	v_subb_co_u32_e32 v37, vcc, v37, v13, vcc
	s_addc_u32 s1, s21, s1
	v_lshl_add_u64 v[32:33], v[6:7], 0, v[32:33]
	v_lshl_add_u64 v[36:37], s[20:21], 0, v[36:37]
	v_lshl_add_u64 v[38:39], s[0:1], 0, v[38:39]
	v_mov_b32_e32 v13, 0
	s_mov_b64 s[0:1], 0
	s_mov_b64 s[10:11], -1
	s_waitcnt lgkmcnt(0)
	s_barrier
	s_load_dwordx2 s[12:13], s[18:19], 0xc0
	v_and_b32_e32 v54, 63, v2
	v_lshrrev_b32_e32 v55, 6, v2
	v_and_b32_e32 v56, 31, v54
	v_lshrrev_b32_e32 v57, 5, v54
	v_lshl_add_u32 v58, v55, 5, v56
	v_lshlrev_b32_e32 v59, 12, v57
	v_lshl_add_u32 v59, v58, 2, v59
	v_mul_u32_u24_e32 v60, 260, v56
	v_lshl_add_u32 v60, v57, 2, v60
	s_lshl_b32 s14, s60, 18
	s_waitcnt vmcnt(0) lgkmcnt(0)
	s_add_u32 s12, s12, s14
	s_addc_u32 s13, s13, 0
	global_load_dword v222, v59, s[12:13] offset:0
	global_load_dword v223, v59, s[12:13] offset:1024
	global_load_dword v224, v59, s[12:13] offset:2048
	global_load_dword v225, v59, s[12:13] offset:3072
	s_add_u32 s12, s12, 0x2000
	s_addc_u32 s13, s13, 0
	global_load_dword v226, v59, s[12:13] offset:0
	global_load_dword v227, v59, s[12:13] offset:1024
	global_load_dword v228, v59, s[12:13] offset:2048
	global_load_dword v229, v59, s[12:13] offset:3072
	s_add_u32 s12, s12, 0x2000
	s_addc_u32 s13, s13, 0
	global_load_dword v230, v59, s[12:13] offset:0
	global_load_dword v231, v59, s[12:13] offset:1024
	global_load_dword v232, v59, s[12:13] offset:2048
	global_load_dword v233, v59, s[12:13] offset:3072
	s_add_u32 s12, s12, 0x2000
	s_addc_u32 s13, s13, 0
	global_load_dword v234, v59, s[12:13] offset:0
	global_load_dword v235, v59, s[12:13] offset:1024
	global_load_dword v236, v59, s[12:13] offset:2048
	global_load_dword v237, v59, s[12:13] offset:3072
	s_add_u32 s12, s12, 0x2000
	s_addc_u32 s13, s13, 0
	global_load_dword v238, v59, s[12:13] offset:0
	global_load_dword v239, v59, s[12:13] offset:1024
	global_load_dword v240, v59, s[12:13] offset:2048
	global_load_dword v241, v59, s[12:13] offset:3072
	s_add_u32 s12, s12, 0x2000
	s_addc_u32 s13, s13, 0
	global_load_dword v242, v59, s[12:13] offset:0
	global_load_dword v243, v59, s[12:13] offset:1024
	global_load_dword v244, v59, s[12:13] offset:2048
	global_load_dword v245, v59, s[12:13] offset:3072
	s_add_u32 s12, s12, 0x2000
	s_addc_u32 s13, s13, 0
	global_load_dword v246, v59, s[12:13] offset:0
	global_load_dword v247, v59, s[12:13] offset:1024
	global_load_dword v248, v59, s[12:13] offset:2048
	global_load_dword v249, v59, s[12:13] offset:3072
	s_add_u32 s12, s12, 0x2000
	s_addc_u32 s13, s13, 0
	global_load_dword v250, v59, s[12:13] offset:0
	global_load_dword v251, v59, s[12:13] offset:1024
	global_load_dword v252, v59, s[12:13] offset:2048
	global_load_dword v253, v59, s[12:13] offset:3072
	s_add_u32 s12, s12, 0x2000
	s_addc_u32 s13, s13, 0
	global_load_dword v200, v59, s[12:13] offset:0
	global_load_dword v201, v59, s[12:13] offset:1024
	global_load_dword v202, v59, s[12:13] offset:2048
	global_load_dword v203, v59, s[12:13] offset:3072
	s_add_u32 s12, s12, 0x2000
	s_addc_u32 s13, s13, 0
	global_load_dword v206, v59, s[12:13] offset:0
	global_load_dword v207, v59, s[12:13] offset:1024
	global_load_dword v208, v59, s[12:13] offset:2048
	global_load_dword v209, v59, s[12:13] offset:3072
	s_add_u32 s12, s12, 0x2000
	s_addc_u32 s13, s13, 0
	global_load_dword v210, v59, s[12:13] offset:0
	global_load_dword v211, v59, s[12:13] offset:1024
	global_load_dword v212, v59, s[12:13] offset:2048
	global_load_dword v213, v59, s[12:13] offset:3072
	s_add_u32 s12, s12, 0x2000
	s_addc_u32 s13, s13, 0
	global_load_dword v214, v59, s[12:13] offset:0
	global_load_dword v215, v59, s[12:13] offset:1024
	global_load_dword v216, v59, s[12:13] offset:2048
	global_load_dword v217, v59, s[12:13] offset:3072
	s_add_u32 s12, s12, 0x2000
	s_addc_u32 s13, s13, 0
	ds_read_b32 v154, v60 offset:12800
	ds_read_b32 v155, v60 offset:12808
	ds_read_b32 v156, v60 offset:12816
	ds_read_b32 v157, v60 offset:12824
	ds_read_b32 v158, v60 offset:12832
	ds_read_b32 v159, v60 offset:12840
	ds_read_b32 v160, v60 offset:12848
	ds_read_b32 v161, v60 offset:12856
	ds_read_b32 v162, v60 offset:12864
	ds_read_b32 v163, v60 offset:12872
	ds_read_b32 v164, v60 offset:12880
	ds_read_b32 v165, v60 offset:12888
	ds_read_b32 v166, v60 offset:12896
	ds_read_b32 v167, v60 offset:12904
	ds_read_b32 v168, v60 offset:12912
	ds_read_b32 v169, v60 offset:12920
	ds_read_b32 v170, v60 offset:12928
	ds_read_b32 v171, v60 offset:12936
	ds_read_b32 v172, v60 offset:12944
	ds_read_b32 v173, v60 offset:12952
	ds_read_b32 v174, v60 offset:12960
	ds_read_b32 v175, v60 offset:12968
	ds_read_b32 v176, v60 offset:12976
	ds_read_b32 v177, v60 offset:12984
	ds_read_b32 v178, v60 offset:12992
	ds_read_b32 v179, v60 offset:13000
	ds_read_b32 v180, v60 offset:13008
	ds_read_b32 v181, v60 offset:13016
	ds_read_b32 v182, v60 offset:13024
	ds_read_b32 v183, v60 offset:13032
	ds_read_b32 v184, v60 offset:13040
	ds_read_b32 v185, v60 offset:13048
	global_load_dword v135, v59, s[12:13] offset:0
	global_load_dword v136, v59, s[12:13] offset:1024
	global_load_dword v137, v59, s[12:13] offset:2048
	global_load_dword v138, v59, s[12:13] offset:3072
	s_add_u32 s12, s12, 0x2000
	s_addc_u32 s13, s13, 0
	global_load_dword v139, v59, s[12:13] offset:0
	global_load_dword v140, v59, s[12:13] offset:1024
	global_load_dword v141, v59, s[12:13] offset:2048
	global_load_dword v142, v59, s[12:13] offset:3072
	s_add_u32 s12, s12, 0x2000
	s_addc_u32 s13, s13, 0
	global_load_dword v143, v59, s[12:13] offset:0
	global_load_dword v144, v59, s[12:13] offset:1024
	global_load_dword v145, v59, s[12:13] offset:2048
	global_load_dword v146, v59, s[12:13] offset:3072
	s_add_u32 s12, s12, 0x2000
	s_addc_u32 s13, s13, 0
	global_load_dword v186, v59, s[12:13] offset:0
	global_load_dword v187, v59, s[12:13] offset:1024
	global_load_dword v188, v59, s[12:13] offset:2048
	global_load_dword v189, v59, s[12:13] offset:3072
	s_add_u32 s12, s12, 0x2000
	s_addc_u32 s13, s13, 0
	s_waitcnt vmcnt(48)
	s_waitcnt lgkmcnt(0)
	v_mfma_f32_32x32x2_f32 v[64:79], v154, v222, 0
	v_mfma_f32_32x32x2_f32 v[80:95], v154, v223, 0
	v_mfma_f32_32x32x2_f32 v[96:111], v154, v224, 0
	v_mfma_f32_32x32x2_f32 v[112:127], v154, v225, 0
	v_mfma_f32_32x32x2_f32 v[64:79], v155, v226, v[64:79]
	v_mfma_f32_32x32x2_f32 v[80:95], v155, v227, v[80:95]
	v_mfma_f32_32x32x2_f32 v[96:111], v155, v228, v[96:111]
	v_mfma_f32_32x32x2_f32 v[112:127], v155, v229, v[112:127]
	v_mfma_f32_32x32x2_f32 v[64:79], v156, v230, v[64:79]
	v_mfma_f32_32x32x2_f32 v[80:95], v156, v231, v[80:95]
	v_mfma_f32_32x32x2_f32 v[96:111], v156, v232, v[96:111]
	v_mfma_f32_32x32x2_f32 v[112:127], v156, v233, v[112:127]
	v_mfma_f32_32x32x2_f32 v[64:79], v157, v234, v[64:79]
	v_mfma_f32_32x32x2_f32 v[80:95], v157, v235, v[80:95]
	v_mfma_f32_32x32x2_f32 v[96:111], v157, v236, v[96:111]
	v_mfma_f32_32x32x2_f32 v[112:127], v157, v237, v[112:127]
	global_load_dword v222, v59, s[12:13] offset:0
	global_load_dword v223, v59, s[12:13] offset:1024
	global_load_dword v224, v59, s[12:13] offset:2048
	global_load_dword v225, v59, s[12:13] offset:3072
	s_add_u32 s12, s12, 0x2000
	s_addc_u32 s13, s13, 0
	global_load_dword v226, v59, s[12:13] offset:0
	global_load_dword v227, v59, s[12:13] offset:1024
	global_load_dword v228, v59, s[12:13] offset:2048
	global_load_dword v229, v59, s[12:13] offset:3072
	s_add_u32 s12, s12, 0x2000
	s_addc_u32 s13, s13, 0
	global_load_dword v230, v59, s[12:13] offset:0
	global_load_dword v231, v59, s[12:13] offset:1024
	global_load_dword v232, v59, s[12:13] offset:2048
	global_load_dword v233, v59, s[12:13] offset:3072
	s_add_u32 s12, s12, 0x2000
	s_addc_u32 s13, s13, 0
	global_load_dword v234, v59, s[12:13] offset:0
	global_load_dword v235, v59, s[12:13] offset:1024
	global_load_dword v236, v59, s[12:13] offset:2048
	global_load_dword v237, v59, s[12:13] offset:3072
	s_add_u32 s12, s12, 0x2000
	s_addc_u32 s13, s13, 0
	s_waitcnt vmcnt(48)
	v_mfma_f32_32x32x2_f32 v[64:79], v158, v238, v[64:79]
	v_mfma_f32_32x32x2_f32 v[80:95], v158, v239, v[80:95]
	v_mfma_f32_32x32x2_f32 v[96:111], v158, v240, v[96:111]
	v_mfma_f32_32x32x2_f32 v[112:127], v158, v241, v[112:127]
	v_mfma_f32_32x32x2_f32 v[64:79], v159, v242, v[64:79]
	v_mfma_f32_32x32x2_f32 v[80:95], v159, v243, v[80:95]
	v_mfma_f32_32x32x2_f32 v[96:111], v159, v244, v[96:111]
	v_mfma_f32_32x32x2_f32 v[112:127], v159, v245, v[112:127]
	v_mfma_f32_32x32x2_f32 v[64:79], v160, v246, v[64:79]
	v_mfma_f32_32x32x2_f32 v[80:95], v160, v247, v[80:95]
	v_mfma_f32_32x32x2_f32 v[96:111], v160, v248, v[96:111]
	v_mfma_f32_32x32x2_f32 v[112:127], v160, v249, v[112:127]
	v_mfma_f32_32x32x2_f32 v[64:79], v161, v250, v[64:79]
	v_mfma_f32_32x32x2_f32 v[80:95], v161, v251, v[80:95]
	v_mfma_f32_32x32x2_f32 v[96:111], v161, v252, v[96:111]
	v_mfma_f32_32x32x2_f32 v[112:127], v161, v253, v[112:127]
	global_load_dword v238, v59, s[12:13] offset:0
	global_load_dword v239, v59, s[12:13] offset:1024
	global_load_dword v240, v59, s[12:13] offset:2048
	global_load_dword v241, v59, s[12:13] offset:3072
	s_add_u32 s12, s12, 0x2000
	s_addc_u32 s13, s13, 0
	global_load_dword v242, v59, s[12:13] offset:0
	global_load_dword v243, v59, s[12:13] offset:1024
	global_load_dword v244, v59, s[12:13] offset:2048
	global_load_dword v245, v59, s[12:13] offset:3072
	s_add_u32 s12, s12, 0x2000
	s_addc_u32 s13, s13, 0
	global_load_dword v246, v59, s[12:13] offset:0
	global_load_dword v247, v59, s[12:13] offset:1024
	global_load_dword v248, v59, s[12:13] offset:2048
	global_load_dword v249, v59, s[12:13] offset:3072
	s_add_u32 s12, s12, 0x2000
	s_addc_u32 s13, s13, 0
	global_load_dword v250, v59, s[12:13] offset:0
	global_load_dword v251, v59, s[12:13] offset:1024
	global_load_dword v252, v59, s[12:13] offset:2048
	global_load_dword v253, v59, s[12:13] offset:3072
	s_add_u32 s12, s12, 0x2000
	s_addc_u32 s13, s13, 0
	s_waitcnt vmcnt(48)
	v_mfma_f32_32x32x2_f32 v[64:79], v162, v200, v[64:79]
	v_mfma_f32_32x32x2_f32 v[80:95], v162, v201, v[80:95]
	v_mfma_f32_32x32x2_f32 v[96:111], v162, v202, v[96:111]
	v_mfma_f32_32x32x2_f32 v[112:127], v162, v203, v[112:127]
	v_mfma_f32_32x32x2_f32 v[64:79], v163, v206, v[64:79]
	v_mfma_f32_32x32x2_f32 v[80:95], v163, v207, v[80:95]
	v_mfma_f32_32x32x2_f32 v[96:111], v163, v208, v[96:111]
	v_mfma_f32_32x32x2_f32 v[112:127], v163, v209, v[112:127]
	v_mfma_f32_32x32x2_f32 v[64:79], v164, v210, v[64:79]
	v_mfma_f32_32x32x2_f32 v[80:95], v164, v211, v[80:95]
	v_mfma_f32_32x32x2_f32 v[96:111], v164, v212, v[96:111]
	v_mfma_f32_32x32x2_f32 v[112:127], v164, v213, v[112:127]
	v_mfma_f32_32x32x2_f32 v[64:79], v165, v214, v[64:79]
	v_mfma_f32_32x32x2_f32 v[80:95], v165, v215, v[80:95]
	v_mfma_f32_32x32x2_f32 v[96:111], v165, v216, v[96:111]
	v_mfma_f32_32x32x2_f32 v[112:127], v165, v217, v[112:127]
	global_load_dword v200, v59, s[12:13] offset:0
	global_load_dword v201, v59, s[12:13] offset:1024
	global_load_dword v202, v59, s[12:13] offset:2048
	global_load_dword v203, v59, s[12:13] offset:3072
	s_add_u32 s12, s12, 0x2000
	s_addc_u32 s13, s13, 0
	global_load_dword v206, v59, s[12:13] offset:0
	global_load_dword v207, v59, s[12:13] offset:1024
	global_load_dword v208, v59, s[12:13] offset:2048
	global_load_dword v209, v59, s[12:13] offset:3072
	s_add_u32 s12, s12, 0x2000
	s_addc_u32 s13, s13, 0
	global_load_dword v210, v59, s[12:13] offset:0
	global_load_dword v211, v59, s[12:13] offset:1024
	global_load_dword v212, v59, s[12:13] offset:2048
	global_load_dword v213, v59, s[12:13] offset:3072
	s_add_u32 s12, s12, 0x2000
	s_addc_u32 s13, s13, 0
	global_load_dword v214, v59, s[12:13] offset:0
	global_load_dword v215, v59, s[12:13] offset:1024
	global_load_dword v216, v59, s[12:13] offset:2048
	global_load_dword v217, v59, s[12:13] offset:3072
	s_add_u32 s12, s12, 0x2000
	s_addc_u32 s13, s13, 0
	s_waitcnt vmcnt(48)
	v_mfma_f32_32x32x2_f32 v[64:79], v166, v135, v[64:79]
	v_mfma_f32_32x32x2_f32 v[80:95], v166, v136, v[80:95]
	v_mfma_f32_32x32x2_f32 v[96:111], v166, v137, v[96:111]
	v_mfma_f32_32x32x2_f32 v[112:127], v166, v138, v[112:127]
	v_mfma_f32_32x32x2_f32 v[64:79], v167, v139, v[64:79]
	v_mfma_f32_32x32x2_f32 v[80:95], v167, v140, v[80:95]
	v_mfma_f32_32x32x2_f32 v[96:111], v167, v141, v[96:111]
	v_mfma_f32_32x32x2_f32 v[112:127], v167, v142, v[112:127]
	v_mfma_f32_32x32x2_f32 v[64:79], v168, v143, v[64:79]
	v_mfma_f32_32x32x2_f32 v[80:95], v168, v144, v[80:95]
	v_mfma_f32_32x32x2_f32 v[96:111], v168, v145, v[96:111]
	v_mfma_f32_32x32x2_f32 v[112:127], v168, v146, v[112:127]
	v_mfma_f32_32x32x2_f32 v[64:79], v169, v186, v[64:79]
	v_mfma_f32_32x32x2_f32 v[80:95], v169, v187, v[80:95]
	v_mfma_f32_32x32x2_f32 v[96:111], v169, v188, v[96:111]
	v_mfma_f32_32x32x2_f32 v[112:127], v169, v189, v[112:127]
	global_load_dword v135, v59, s[12:13] offset:0
	global_load_dword v136, v59, s[12:13] offset:1024
	global_load_dword v137, v59, s[12:13] offset:2048
	global_load_dword v138, v59, s[12:13] offset:3072
	s_add_u32 s12, s12, 0x2000
	s_addc_u32 s13, s13, 0
	global_load_dword v139, v59, s[12:13] offset:0
	global_load_dword v140, v59, s[12:13] offset:1024
	global_load_dword v141, v59, s[12:13] offset:2048
	global_load_dword v142, v59, s[12:13] offset:3072
	s_add_u32 s12, s12, 0x2000
	s_addc_u32 s13, s13, 0
	global_load_dword v143, v59, s[12:13] offset:0
	global_load_dword v144, v59, s[12:13] offset:1024
	global_load_dword v145, v59, s[12:13] offset:2048
	global_load_dword v146, v59, s[12:13] offset:3072
	s_add_u32 s12, s12, 0x2000
	s_addc_u32 s13, s13, 0
	global_load_dword v186, v59, s[12:13] offset:0
	global_load_dword v187, v59, s[12:13] offset:1024
	global_load_dword v188, v59, s[12:13] offset:2048
	global_load_dword v189, v59, s[12:13] offset:3072
	s_add_u32 s12, s12, 0x2000
	s_addc_u32 s13, s13, 0
	s_waitcnt vmcnt(48)
	v_mfma_f32_32x32x2_f32 v[64:79], v170, v222, v[64:79]
	v_mfma_f32_32x32x2_f32 v[80:95], v170, v223, v[80:95]
	v_mfma_f32_32x32x2_f32 v[96:111], v170, v224, v[96:111]
	v_mfma_f32_32x32x2_f32 v[112:127], v170, v225, v[112:127]
	v_mfma_f32_32x32x2_f32 v[64:79], v171, v226, v[64:79]
	v_mfma_f32_32x32x2_f32 v[80:95], v171, v227, v[80:95]
	v_mfma_f32_32x32x2_f32 v[96:111], v171, v228, v[96:111]
	v_mfma_f32_32x32x2_f32 v[112:127], v171, v229, v[112:127]
	v_mfma_f32_32x32x2_f32 v[64:79], v172, v230, v[64:79]
	v_mfma_f32_32x32x2_f32 v[80:95], v172, v231, v[80:95]
	v_mfma_f32_32x32x2_f32 v[96:111], v172, v232, v[96:111]
	v_mfma_f32_32x32x2_f32 v[112:127], v172, v233, v[112:127]
	v_mfma_f32_32x32x2_f32 v[64:79], v173, v234, v[64:79]
	v_mfma_f32_32x32x2_f32 v[80:95], v173, v235, v[80:95]
	v_mfma_f32_32x32x2_f32 v[96:111], v173, v236, v[96:111]
	v_mfma_f32_32x32x2_f32 v[112:127], v173, v237, v[112:127]
	s_waitcnt vmcnt(32)
	v_mfma_f32_32x32x2_f32 v[64:79], v174, v238, v[64:79]
	v_mfma_f32_32x32x2_f32 v[80:95], v174, v239, v[80:95]
	v_mfma_f32_32x32x2_f32 v[96:111], v174, v240, v[96:111]
	v_mfma_f32_32x32x2_f32 v[112:127], v174, v241, v[112:127]
	v_mfma_f32_32x32x2_f32 v[64:79], v175, v242, v[64:79]
	v_mfma_f32_32x32x2_f32 v[80:95], v175, v243, v[80:95]
	v_mfma_f32_32x32x2_f32 v[96:111], v175, v244, v[96:111]
	v_mfma_f32_32x32x2_f32 v[112:127], v175, v245, v[112:127]
	v_mfma_f32_32x32x2_f32 v[64:79], v176, v246, v[64:79]
	v_mfma_f32_32x32x2_f32 v[80:95], v176, v247, v[80:95]
	v_mfma_f32_32x32x2_f32 v[96:111], v176, v248, v[96:111]
	v_mfma_f32_32x32x2_f32 v[112:127], v176, v249, v[112:127]
	v_mfma_f32_32x32x2_f32 v[64:79], v177, v250, v[64:79]
	v_mfma_f32_32x32x2_f32 v[80:95], v177, v251, v[80:95]
	v_mfma_f32_32x32x2_f32 v[96:111], v177, v252, v[96:111]
	v_mfma_f32_32x32x2_f32 v[112:127], v177, v253, v[112:127]
	s_waitcnt vmcnt(16)
	v_mfma_f32_32x32x2_f32 v[64:79], v178, v200, v[64:79]
	v_mfma_f32_32x32x2_f32 v[80:95], v178, v201, v[80:95]
	v_mfma_f32_32x32x2_f32 v[96:111], v178, v202, v[96:111]
	v_mfma_f32_32x32x2_f32 v[112:127], v178, v203, v[112:127]
	v_mfma_f32_32x32x2_f32 v[64:79], v179, v206, v[64:79]
	v_mfma_f32_32x32x2_f32 v[80:95], v179, v207, v[80:95]
	v_mfma_f32_32x32x2_f32 v[96:111], v179, v208, v[96:111]
	v_mfma_f32_32x32x2_f32 v[112:127], v179, v209, v[112:127]
	v_mfma_f32_32x32x2_f32 v[64:79], v180, v210, v[64:79]
	v_mfma_f32_32x32x2_f32 v[80:95], v180, v211, v[80:95]
	v_mfma_f32_32x32x2_f32 v[96:111], v180, v212, v[96:111]
	v_mfma_f32_32x32x2_f32 v[112:127], v180, v213, v[112:127]
	v_mfma_f32_32x32x2_f32 v[64:79], v181, v214, v[64:79]
	v_mfma_f32_32x32x2_f32 v[80:95], v181, v215, v[80:95]
	v_mfma_f32_32x32x2_f32 v[96:111], v181, v216, v[96:111]
	v_mfma_f32_32x32x2_f32 v[112:127], v181, v217, v[112:127]
	s_waitcnt vmcnt(0)
	v_mfma_f32_32x32x2_f32 v[64:79], v182, v135, v[64:79]
	v_mfma_f32_32x32x2_f32 v[80:95], v182, v136, v[80:95]
	v_mfma_f32_32x32x2_f32 v[96:111], v182, v137, v[96:111]
	v_mfma_f32_32x32x2_f32 v[112:127], v182, v138, v[112:127]
	v_mfma_f32_32x32x2_f32 v[64:79], v183, v139, v[64:79]
	v_mfma_f32_32x32x2_f32 v[80:95], v183, v140, v[80:95]
	v_mfma_f32_32x32x2_f32 v[96:111], v183, v141, v[96:111]
	v_mfma_f32_32x32x2_f32 v[112:127], v183, v142, v[112:127]
	v_mfma_f32_32x32x2_f32 v[64:79], v184, v143, v[64:79]
	v_mfma_f32_32x32x2_f32 v[80:95], v184, v144, v[80:95]
	v_mfma_f32_32x32x2_f32 v[96:111], v184, v145, v[96:111]
	v_mfma_f32_32x32x2_f32 v[112:127], v184, v146, v[112:127]
	v_mfma_f32_32x32x2_f32 v[64:79], v185, v186, v[64:79]
	v_mfma_f32_32x32x2_f32 v[80:95], v185, v187, v[80:95]
	v_mfma_f32_32x32x2_f32 v[96:111], v185, v188, v[96:111]
	v_mfma_f32_32x32x2_f32 v[112:127], v185, v189, v[112:127]
	v_cvt_f32_u32_e32 v32, v58
	v_add_u32_e32 v33, 0x100, v58
	v_cvt_f32_u32_e32 v33, v33
	v_mov_b32_e32 v40, 0xc0447cbd
	v_mov_b32_e32 v41, 0xc0447cbd
	v_fmac_f32_e32 v40, 0xbcc4df2d, v32
	v_fmac_f32_e32 v41, 0xbcc4df2d, v33
	v_rcp_f32_e32 v42, v9
	v_and_b32_e32 v40, 0x7fffffff, v40
	v_and_b32_e32 v41, 0x7fffffff, v41
	v_mul_f32_e32 v40, 0x3fb8aa3b, v40
	v_mul_f32_e32 v41, 0x3fb8aa3b, v41
	v_mul_f32_e64 v40, -v40, v42
	v_mul_f32_e64 v41, -v41, v42
	v_lshl_add_u32 v43, v57, 2, s56
	v_cvt_f32_u32_e32 v128, v43
	s_and_b64 s[0:1], s[58:59], exec
	s_movk_i32 s28, 0x2000
	s_cselect_b32 s28, 0x400, s28
	v_sub_u32_e32 v32, v58, v2
	v_mov_b32_e32 v33, s28
	v_mad_i64_i32 v[36:37], s[0:1], v32, v33, v[34:35]
	s_lshl_b32 s14, s56, 1
	v_lshl_add_u32 v38, v57, 3, s14
	v_mov_b32_e32 v39, 0
	v_sub_co_u32_e32 v32, vcc, v36, v38
	s_nop 1
	v_subb_co_u32_e32 v33, vcc, v37, v39, vcc
	v_lshl_add_u64 v[34:35], v[36:37], 0, v[38:39]
	s_lshl_b32 s14, s28, 8
	s_mov_b32 s15, 0
	v_lshl_add_u64 v[36:37], v[32:33], 0, s[14:15]
	v_lshl_add_u64 v[38:39], v[34:35], 0, s[14:15]
	v_mul_f32_e32 v130, v128, v40
	v_mul_f32_e32 v131, v128, v41
	v_exp_f32_e32 v154, v130
	v_exp_f32_e32 v170, v131
	v_add_f32_e32 v129, 0x3f800000, v128
	v_mul_f32_e32 v130, v129, v40
	v_mul_f32_e32 v131, v129, v41
	v_exp_f32_e32 v155, v130
	v_exp_f32_e32 v171, v131
	v_add_f32_e32 v129, 0x40000000, v128
	v_mul_f32_e32 v130, v129, v40
	v_mul_f32_e32 v131, v129, v41
	v_exp_f32_e32 v156, v130
	v_exp_f32_e32 v172, v131
	v_add_f32_e32 v129, 0x40400000, v128
	v_mul_f32_e32 v130, v129, v40
	v_mul_f32_e32 v131, v129, v41
	v_exp_f32_e32 v157, v130
	v_exp_f32_e32 v173, v131
	v_add_f32_e32 v129, 0x41000000, v128
	v_mul_f32_e32 v130, v129, v40
	v_mul_f32_e32 v131, v129, v41
	v_exp_f32_e32 v158, v130
	v_exp_f32_e32 v174, v131
	v_add_f32_e32 v129, 0x41100000, v128
	v_mul_f32_e32 v130, v129, v40
	v_mul_f32_e32 v131, v129, v41
	v_exp_f32_e32 v159, v130
	v_exp_f32_e32 v175, v131
	v_add_f32_e32 v129, 0x41200000, v128
	v_mul_f32_e32 v130, v129, v40
	v_mul_f32_e32 v131, v129, v41
	v_exp_f32_e32 v160, v130
	v_exp_f32_e32 v176, v131
	v_add_f32_e32 v129, 0x41300000, v128
	v_mul_f32_e32 v130, v129, v40
	v_mul_f32_e32 v131, v129, v41
	v_exp_f32_e32 v161, v130
	v_exp_f32_e32 v177, v131
	v_add_f32_e32 v129, 0x41800000, v128
	v_mul_f32_e32 v130, v129, v40
	v_mul_f32_e32 v131, v129, v41
	v_exp_f32_e32 v162, v130
	v_exp_f32_e32 v178, v131
	v_add_f32_e32 v129, 0x41880000, v128
	v_mul_f32_e32 v130, v129, v40
	v_mul_f32_e32 v131, v129, v41
	v_exp_f32_e32 v163, v130
	v_exp_f32_e32 v179, v131
	v_add_f32_e32 v129, 0x41900000, v128
	v_mul_f32_e32 v130, v129, v40
	v_mul_f32_e32 v131, v129, v41
	v_exp_f32_e32 v164, v130
	v_exp_f32_e32 v180, v131
	v_add_f32_e32 v129, 0x41980000, v128
	v_mul_f32_e32 v130, v129, v40
	v_mul_f32_e32 v131, v129, v41
	v_exp_f32_e32 v165, v130
	v_exp_f32_e32 v181, v131
	v_add_f32_e32 v129, 0x41c00000, v128
	v_mul_f32_e32 v130, v129, v40
	v_mul_f32_e32 v131, v129, v41
	v_exp_f32_e32 v166, v130
	v_exp_f32_e32 v182, v131
	v_add_f32_e32 v129, 0x41c80000, v128
	v_mul_f32_e32 v130, v129, v40
	v_mul_f32_e32 v131, v129, v41
	v_exp_f32_e32 v167, v130
	v_exp_f32_e32 v183, v131
	v_add_f32_e32 v129, 0x41d00000, v128
	v_mul_f32_e32 v130, v129, v40
	v_mul_f32_e32 v131, v129, v41
	v_exp_f32_e32 v168, v130
	v_exp_f32_e32 v184, v131
	v_add_f32_e32 v129, 0x41d80000, v128
	v_mul_f32_e32 v130, v129, v40
	v_mul_f32_e32 v131, v129, v41
	v_exp_f32_e32 v169, v130
	v_exp_f32_e32 v185, v131
	s_nop 15
	s_nop 7
	v_mul_f32_e32 v64, v64, v154
	v_mul_f32_e32 v96, v96, v154
	v_mul_f32_e32 v80, v80, v170
	v_mul_f32_e32 v112, v112, v170
	v_mul_f32_e32 v65, v65, v155
	v_mul_f32_e32 v97, v97, v155
	v_mul_f32_e32 v81, v81, v171
	v_mul_f32_e32 v113, v113, v171
	v_mul_f32_e32 v66, v66, v156
	v_mul_f32_e32 v98, v98, v156
	v_mul_f32_e32 v82, v82, v172
	v_mul_f32_e32 v114, v114, v172
	v_mul_f32_e32 v67, v67, v157
	v_mul_f32_e32 v99, v99, v157
	v_mul_f32_e32 v83, v83, v173
	v_mul_f32_e32 v115, v115, v173
	v_mul_f32_e32 v68, v68, v158
	v_mul_f32_e32 v100, v100, v158
	v_mul_f32_e32 v84, v84, v174
	v_mul_f32_e32 v116, v116, v174
	v_mul_f32_e32 v69, v69, v159
	v_mul_f32_e32 v101, v101, v159
	v_mul_f32_e32 v85, v85, v175
	v_mul_f32_e32 v117, v117, v175
	v_mul_f32_e32 v70, v70, v160
	v_mul_f32_e32 v102, v102, v160
	v_mul_f32_e32 v86, v86, v176
	v_mul_f32_e32 v118, v118, v176
	v_mul_f32_e32 v71, v71, v161
	v_mul_f32_e32 v103, v103, v161
	v_mul_f32_e32 v87, v87, v177
	v_mul_f32_e32 v119, v119, v177
	v_mul_f32_e32 v72, v72, v162
	v_mul_f32_e32 v104, v104, v162
	v_mul_f32_e32 v88, v88, v178
	v_mul_f32_e32 v120, v120, v178
	v_mul_f32_e32 v73, v73, v163
	v_mul_f32_e32 v105, v105, v163
	v_mul_f32_e32 v89, v89, v179
	v_mul_f32_e32 v121, v121, v179
	v_mul_f32_e32 v74, v74, v164
	v_mul_f32_e32 v106, v106, v164
	v_mul_f32_e32 v90, v90, v180
	v_mul_f32_e32 v122, v122, v180
	v_mul_f32_e32 v75, v75, v165
	v_mul_f32_e32 v107, v107, v165
	v_mul_f32_e32 v91, v91, v181
	v_mul_f32_e32 v123, v123, v181
	v_mul_f32_e32 v76, v76, v166
	v_mul_f32_e32 v108, v108, v166
	v_mul_f32_e32 v92, v92, v182
	v_mul_f32_e32 v124, v124, v182
	v_mul_f32_e32 v77, v77, v167
	v_mul_f32_e32 v109, v109, v167
	v_mul_f32_e32 v93, v93, v183
	v_mul_f32_e32 v125, v125, v183
	v_mul_f32_e32 v78, v78, v168
	v_mul_f32_e32 v110, v110, v168
	v_mul_f32_e32 v94, v94, v184
	v_mul_f32_e32 v126, v126, v184
	v_mul_f32_e32 v79, v79, v169
	v_mul_f32_e32 v111, v111, v169
	v_mul_f32_e32 v95, v95, v185
	v_mul_f32_e32 v127, v127, v185
	v_cmp_eq_u32_e32 vcc, 0, v43
	v_add_f32_e32 v129, v64, v96
	v_add_f32_e32 v130, v80, v112
	s_nop 1
	v_cndmask_b32_e32 v64, v64, v129, vcc
	v_cndmask_b32_e32 v96, v96, v129, vcc
	v_cndmask_b32_e32 v80, v80, v130, vcc
	v_cndmask_b32_e32 v112, v112, v130, vcc
	v_cvt_pk_bf16_f32 v64, v64, v64
	v_cvt_pk_bf16_f32 v80, v80, v80
	v_cvt_pk_bf16_f32 v96, v96, v96
	v_cvt_pk_bf16_f32 v112, v112, v112
	global_store_short v[32:33], v64, off
	global_store_short v[36:37], v80, off
	global_store_short v[34:35], v96, off
	global_store_short v[38:39], v112, off
	v_cvt_pk_bf16_f32 v65, v65, v65
	v_cvt_pk_bf16_f32 v81, v81, v81
	v_cvt_pk_bf16_f32 v97, v97, v97
	v_cvt_pk_bf16_f32 v113, v113, v113
	global_store_short v[32:33], v65, off offset:-2
	global_store_short v[36:37], v81, off offset:-2
	global_store_short v[34:35], v97, off offset:2
	global_store_short v[38:39], v113, off offset:2
	v_cvt_pk_bf16_f32 v66, v66, v66
	v_cvt_pk_bf16_f32 v82, v82, v82
	v_cvt_pk_bf16_f32 v98, v98, v98
	v_cvt_pk_bf16_f32 v114, v114, v114
	global_store_short v[32:33], v66, off offset:-4
	global_store_short v[36:37], v82, off offset:-4
	global_store_short v[34:35], v98, off offset:4
	global_store_short v[38:39], v114, off offset:4
	v_cvt_pk_bf16_f32 v67, v67, v67
	v_cvt_pk_bf16_f32 v83, v83, v83
	v_cvt_pk_bf16_f32 v99, v99, v99
	v_cvt_pk_bf16_f32 v115, v115, v115
	global_store_short v[32:33], v67, off offset:-6
	global_store_short v[36:37], v83, off offset:-6
	global_store_short v[34:35], v99, off offset:6
	global_store_short v[38:39], v115, off offset:6
	v_cvt_pk_bf16_f32 v68, v68, v68
	v_cvt_pk_bf16_f32 v84, v84, v84
	v_cvt_pk_bf16_f32 v100, v100, v100
	v_cvt_pk_bf16_f32 v116, v116, v116
	global_store_short v[32:33], v68, off offset:-16
	global_store_short v[36:37], v84, off offset:-16
	global_store_short v[34:35], v100, off offset:16
	global_store_short v[38:39], v116, off offset:16
	v_cvt_pk_bf16_f32 v69, v69, v69
	v_cvt_pk_bf16_f32 v85, v85, v85
	v_cvt_pk_bf16_f32 v101, v101, v101
	v_cvt_pk_bf16_f32 v117, v117, v117
	global_store_short v[32:33], v69, off offset:-18
	global_store_short v[36:37], v85, off offset:-18
	global_store_short v[34:35], v101, off offset:18
	global_store_short v[38:39], v117, off offset:18
	v_cvt_pk_bf16_f32 v70, v70, v70
	v_cvt_pk_bf16_f32 v86, v86, v86
	v_cvt_pk_bf16_f32 v102, v102, v102
	v_cvt_pk_bf16_f32 v118, v118, v118
	global_store_short v[32:33], v70, off offset:-20
	global_store_short v[36:37], v86, off offset:-20
	global_store_short v[34:35], v102, off offset:20
	global_store_short v[38:39], v118, off offset:20
	v_cvt_pk_bf16_f32 v71, v71, v71
	v_cvt_pk_bf16_f32 v87, v87, v87
	v_cvt_pk_bf16_f32 v103, v103, v103
	v_cvt_pk_bf16_f32 v119, v119, v119
	global_store_short v[32:33], v71, off offset:-22
	global_store_short v[36:37], v87, off offset:-22
	global_store_short v[34:35], v103, off offset:22
	global_store_short v[38:39], v119, off offset:22
	v_cvt_pk_bf16_f32 v72, v72, v72
	v_cvt_pk_bf16_f32 v88, v88, v88
	v_cvt_pk_bf16_f32 v104, v104, v104
	v_cvt_pk_bf16_f32 v120, v120, v120
	global_store_short v[32:33], v72, off offset:-32
	global_store_short v[36:37], v88, off offset:-32
	global_store_short v[34:35], v104, off offset:32
	global_store_short v[38:39], v120, off offset:32
	v_cvt_pk_bf16_f32 v73, v73, v73
	v_cvt_pk_bf16_f32 v89, v89, v89
	v_cvt_pk_bf16_f32 v105, v105, v105
	v_cvt_pk_bf16_f32 v121, v121, v121
	global_store_short v[32:33], v73, off offset:-34
	global_store_short v[36:37], v89, off offset:-34
	global_store_short v[34:35], v105, off offset:34
	global_store_short v[38:39], v121, off offset:34
	v_cvt_pk_bf16_f32 v74, v74, v74
	v_cvt_pk_bf16_f32 v90, v90, v90
	v_cvt_pk_bf16_f32 v106, v106, v106
	v_cvt_pk_bf16_f32 v122, v122, v122
	global_store_short v[32:33], v74, off offset:-36
	global_store_short v[36:37], v90, off offset:-36
	global_store_short v[34:35], v106, off offset:36
	global_store_short v[38:39], v122, off offset:36
	v_cvt_pk_bf16_f32 v75, v75, v75
	v_cvt_pk_bf16_f32 v91, v91, v91
	v_cvt_pk_bf16_f32 v107, v107, v107
	v_cvt_pk_bf16_f32 v123, v123, v123
	global_store_short v[32:33], v75, off offset:-38
	global_store_short v[36:37], v91, off offset:-38
	global_store_short v[34:35], v107, off offset:38
	global_store_short v[38:39], v123, off offset:38
	v_cvt_pk_bf16_f32 v76, v76, v76
	v_cvt_pk_bf16_f32 v92, v92, v92
	v_cvt_pk_bf16_f32 v108, v108, v108
	v_cvt_pk_bf16_f32 v124, v124, v124
	global_store_short v[32:33], v76, off offset:-48
	global_store_short v[36:37], v92, off offset:-48
	global_store_short v[34:35], v108, off offset:48
	global_store_short v[38:39], v124, off offset:48
	v_cvt_pk_bf16_f32 v77, v77, v77
	v_cvt_pk_bf16_f32 v93, v93, v93
	v_cvt_pk_bf16_f32 v109, v109, v109
	v_cvt_pk_bf16_f32 v125, v125, v125
	global_store_short v[32:33], v77, off offset:-50
	global_store_short v[36:37], v93, off offset:-50
	global_store_short v[34:35], v109, off offset:50
	global_store_short v[38:39], v125, off offset:50
	v_cvt_pk_bf16_f32 v78, v78, v78
	v_cvt_pk_bf16_f32 v94, v94, v94
	v_cvt_pk_bf16_f32 v110, v110, v110
	v_cvt_pk_bf16_f32 v126, v126, v126
	global_store_short v[32:33], v78, off offset:-52
	global_store_short v[36:37], v94, off offset:-52
	global_store_short v[34:35], v110, off offset:52
	global_store_short v[38:39], v126, off offset:52
	v_cvt_pk_bf16_f32 v79, v79, v79
	v_cvt_pk_bf16_f32 v95, v95, v95
	v_cvt_pk_bf16_f32 v111, v111, v111
	v_cvt_pk_bf16_f32 v127, v127, v127
	global_store_short v[32:33], v79, off offset:-54
	global_store_short v[36:37], v95, off offset:-54
	global_store_short v[34:35], v111, off offset:54
	global_store_short v[38:39], v127, off offset:54
	s_branch .LBB0_75
